# P10 MoE-down K-loop: peel first iteration after a unit switch with vmcnt relaxed by the 8 epilogue stores (no store drain at unit switch)
# speedup vs baseline: 1.1117x; 1.1117x over previous
.LBB0_1434:
	s_lshr_b32 s1, s1, 25
	s_and_b32 s23, s16, 3
	s_add_i32 s1, s0, s1
	s_ashr_i32 s49, s1, 7
	s_lshl_b32 s1, s22, 13
	s_lshl_b32 s20, s23, 12
	s_add_u32 s16, s26, 0x1eb00080
	s_mov_b64 s[18:19], 0x80
	s_addc_u32 s17, s27, 0
	v_lshl_add_u64 v[8:9], v[8:9], 0, s[18:19]
	s_add_i32 m0, s29, 0x18000
	s_waitcnt vmcnt(2)
	s_barrier
	global_load_lds_dwordx4 v[8:9], off
	v_lshl_add_u64 v[6:7], v[6:7], 0, s[18:19]
	s_add_i32 m0, s29, 0x1a000
	s_add_i32 s50, s29, 0x8000
	global_load_lds_dwordx4 v[6:7], off
	v_lshl_add_u64 v[6:7], s[16:17], 0, v[168:169]
	s_mov_b32 m0, s50
	s_add_i32 s51, s29, 0xa000
	global_load_lds_dwordx4 v[6:7], off
	v_lshl_add_u64 v[6:7], s[16:17], 0, v[170:171]
	s_mov_b32 m0, s51
	v_lshl_add_u64 v[4:5], v[4:5], 0, s[18:19]
	global_load_lds_dwordx4 v[6:7], off
	s_add_i32 m0, s29, 0x1c000
	v_lshl_add_u64 v[2:3], v[2:3], 0, s[18:19]
	global_load_lds_dwordx4 v[4:5], off
	s_add_i32 m0, s29, 0x1e000
	v_lshlrev_b32_e32 v4, 2, v0
	global_load_lds_dwordx4 v[2:3], off
	v_and_b32_e32 v2, 15, v0
	s_ashr_i32 s52, s62, 3
	v_and_b32_e32 v4, 32, v4
	v_lshl_or_b32 v5, v2, 6, v10
	s_cmpk_gt_i32 s0, 0x7f
	v_lshlrev_b32_e32 v3, 6, v0
	s_movk_i32 s21, 0x3c0
	v_bitop3_b32 v5, v5, s1, v4 bitop3:0xde
	s_cselect_b64 s[0:1], -1, 0
	s_add_i32 s54, s49, -2
	v_and_or_b32 v3, v3, s21, v10
	s_cmpk_lt_u32 s3, 0x100
	v_bitop3_b32 v3, s20, v3, v4 bitop3:0xf6
	s_waitcnt vmcnt(6)
	s_cselect_b64 s[20:21], -1, 0
	v_lshlrev_b32_e32 v2, 11, v2
	s_add_i32 s57, 0, 0x10000
	s_add_i32 s59, 0, 0x14000
	s_add_i32 s61, 0, 0x18000
	v_lshl_or_b32 v171, s22, 17, v2
	v_cndmask_b32_e64 v2, 0, 1, s[0:1]
	v_add_u32_e32 v191, s57, v3
	v_add_u32_e32 v192, s59, v3
	s_add_i32 s57, s57, s2
	s_add_i32 s59, s59, s2
	v_add_u32_e32 v194, s61, v3
	s_add_i32 s63, 0, 0x1c000
	s_add_i32 s61, s61, s2
	s_mov_b32 s68, s62
	s_mov_b32 s53, 0
	v_lshl_or_b32 v190, s23, 6, v10
	v_cmp_ne_u32_e64 s[0:1], 1, v2
	v_add_u32_e32 v193, 0, v5
	s_add_i32 s55, s29, 0xc000
	s_add_i32 s56, s29, 0xe000
	s_add_i32 s58, s57, 0x2000
	s_add_i32 s60, s59, 0x2000
	v_add_u32_e32 v195, s63, v3
	s_add_i32 s62, s61, 0x2000
	s_add_i32 s63, s63, s2
	s_mov_b32 s64, 0xc3e00000
	v_mov_b32_e32 v196, 0x43e00000
	v_mov_b32_e32 v197, v168
	s_barrier
	s_mov_b32 s98, 0
	s_branch .LBB0_1437

.LBB0_1441:
	v_mov_b32_e32 v161, 0
	s_and_b64 vcc, exec, s[0:1]
	v_mov_b32_e32 v160, v161
	v_mov_b32_e32 v159, v161
	v_mov_b32_e32 v158, v161
	v_mov_b32_e32 v157, v161
	v_mov_b32_e32 v156, v161
	v_mov_b32_e32 v155, v161
	v_mov_b32_e32 v154, v161
	v_mov_b32_e32 v145, v161
	v_mov_b32_e32 v144, v161
	v_mov_b32_e32 v143, v161
	v_mov_b32_e32 v142, v161
	v_mov_b32_e32 v141, v161
	v_mov_b32_e32 v140, v161
	v_mov_b32_e32 v139, v161
	v_mov_b32_e32 v138, v161
	v_mov_b32_e32 v129, v161
	v_mov_b32_e32 v128, v161
	v_mov_b32_e32 v127, v161
	v_mov_b32_e32 v126, v161
	v_mov_b32_e32 v125, v161
	v_mov_b32_e32 v124, v161
	v_mov_b32_e32 v123, v161
	v_mov_b32_e32 v122, v161
	v_mov_b32_e32 v113, v161
	v_mov_b32_e32 v112, v161
	v_mov_b32_e32 v111, v161
	v_mov_b32_e32 v110, v161
	v_mov_b32_e32 v109, v161
	v_mov_b32_e32 v108, v161
	v_mov_b32_e32 v107, v161
	v_mov_b32_e32 v106, v161
	v_mov_b32_e32 v153, v161
	v_mov_b32_e32 v152, v161
	v_mov_b32_e32 v151, v161
	v_mov_b32_e32 v150, v161
	v_mov_b32_e32 v149, v161
	v_mov_b32_e32 v148, v161
	v_mov_b32_e32 v147, v161
	v_mov_b32_e32 v146, v161
	v_mov_b32_e32 v137, v161
	v_mov_b32_e32 v136, v161
	v_mov_b32_e32 v135, v161
	v_mov_b32_e32 v134, v161
	v_mov_b32_e32 v133, v161
	v_mov_b32_e32 v132, v161
	v_mov_b32_e32 v131, v161
	v_mov_b32_e32 v130, v161
	v_mov_b32_e32 v121, v161
	v_mov_b32_e32 v120, v161
	v_mov_b32_e32 v119, v161
	v_mov_b32_e32 v118, v161
	v_mov_b32_e32 v117, v161
	v_mov_b32_e32 v116, v161
	v_mov_b32_e32 v115, v161
	v_mov_b32_e32 v114, v161
	v_mov_b32_e32 v105, v161
	v_mov_b32_e32 v104, v161
	v_mov_b32_e32 v103, v161
	v_mov_b32_e32 v102, v161
	v_mov_b32_e32 v101, v161
	v_mov_b32_e32 v100, v161
	v_mov_b32_e32 v99, v161
	v_mov_b32_e32 v98, v161
	v_mov_b32_e32 v97, v161
	v_mov_b32_e32 v96, v161
	v_mov_b32_e32 v95, v161
	v_mov_b32_e32 v94, v161
	v_mov_b32_e32 v93, v161
	v_mov_b32_e32 v92, v161
	v_mov_b32_e32 v91, v161
	v_mov_b32_e32 v90, v161
	v_mov_b32_e32 v81, v161
	v_mov_b32_e32 v80, v161
	v_mov_b32_e32 v79, v161
	v_mov_b32_e32 v78, v161
	v_mov_b32_e32 v77, v161
	v_mov_b32_e32 v76, v161
	v_mov_b32_e32 v75, v161
	v_mov_b32_e32 v74, v161
	v_mov_b32_e32 v65, v161
	v_mov_b32_e32 v64, v161
	v_mov_b32_e32 v63, v161
	v_mov_b32_e32 v62, v161
	v_mov_b32_e32 v61, v161
	v_mov_b32_e32 v60, v161
	v_mov_b32_e32 v59, v161
	v_mov_b32_e32 v58, v161
	v_mov_b32_e32 v49, v161
	v_mov_b32_e32 v48, v161
	v_mov_b32_e32 v47, v161
	v_mov_b32_e32 v46, v161
	v_mov_b32_e32 v45, v161
	v_mov_b32_e32 v44, v161
	v_mov_b32_e32 v43, v161
	v_mov_b32_e32 v42, v161
	v_mov_b32_e32 v89, v161
	v_mov_b32_e32 v88, v161
	v_mov_b32_e32 v87, v161
	v_mov_b32_e32 v86, v161
	v_mov_b32_e32 v85, v161
	v_mov_b32_e32 v84, v161
	v_mov_b32_e32 v83, v161
	v_mov_b32_e32 v82, v161
	v_mov_b32_e32 v73, v161
	v_mov_b32_e32 v72, v161
	v_mov_b32_e32 v71, v161
	v_mov_b32_e32 v70, v161
	v_mov_b32_e32 v69, v161
	v_mov_b32_e32 v68, v161
	v_mov_b32_e32 v67, v161
	v_mov_b32_e32 v66, v161
	v_mov_b32_e32 v57, v161
	v_mov_b32_e32 v56, v161
	v_mov_b32_e32 v55, v161
	v_mov_b32_e32 v54, v161
	v_mov_b32_e32 v53, v161
	v_mov_b32_e32 v52, v161
	v_mov_b32_e32 v51, v161
	v_mov_b32_e32 v50, v161
	v_mov_b32_e32 v41, v161
	v_mov_b32_e32 v40, v161
	v_mov_b32_e32 v39, v161
	v_mov_b32_e32 v38, v161
	v_mov_b32_e32 v37, v161
	v_mov_b32_e32 v36, v161
	v_mov_b32_e32 v35, v161
	v_mov_b32_e32 v34, v161
	s_cbranch_vccnz .LBB0_1444
	v_mov_b32_e32 v34, 0
	v_mov_b32_e32 v175, v169
	v_mov_b32_e32 v173, v169
	s_mov_b32 s23, 0
	s_mov_b64 s[34:35], 0x100
	s_mov_b64 s[36:37], s[16:17]
	v_mov_b32_e32 v35, v34
	v_mov_b32_e32 v36, v34
	v_mov_b32_e32 v37, v34
	v_mov_b32_e32 v38, v34
	v_mov_b32_e32 v39, v34
	v_mov_b32_e32 v40, v34
	v_mov_b32_e32 v41, v34
	v_mov_b32_e32 v50, v34
	v_mov_b32_e32 v51, v34
	v_mov_b32_e32 v52, v34
	v_mov_b32_e32 v53, v34
	v_mov_b32_e32 v54, v34
	v_mov_b32_e32 v55, v34
	v_mov_b32_e32 v56, v34
	v_mov_b32_e32 v57, v34
	v_mov_b32_e32 v66, v34
	v_mov_b32_e32 v67, v34
	v_mov_b32_e32 v68, v34
	v_mov_b32_e32 v69, v34
	v_mov_b32_e32 v70, v34
	v_mov_b32_e32 v71, v34
	v_mov_b32_e32 v72, v34
	v_mov_b32_e32 v73, v34
	v_mov_b32_e32 v82, v34
	v_mov_b32_e32 v83, v34
	v_mov_b32_e32 v84, v34
	v_mov_b32_e32 v85, v34
	v_mov_b32_e32 v86, v34
	v_mov_b32_e32 v87, v34
	v_mov_b32_e32 v88, v34
	v_mov_b32_e32 v89, v34
	v_mov_b32_e32 v42, v34
	v_mov_b32_e32 v43, v34
	v_mov_b32_e32 v44, v34
	v_mov_b32_e32 v45, v34
	v_mov_b32_e32 v46, v34
	v_mov_b32_e32 v47, v34
	v_mov_b32_e32 v48, v34
	v_mov_b32_e32 v49, v34
	v_mov_b32_e32 v58, v34
	v_mov_b32_e32 v59, v34
	v_mov_b32_e32 v60, v34
	v_mov_b32_e32 v61, v34
	v_mov_b32_e32 v62, v34
	v_mov_b32_e32 v63, v34
	v_mov_b32_e32 v64, v34
	v_mov_b32_e32 v65, v34
	v_mov_b32_e32 v74, v34
	v_mov_b32_e32 v75, v34
	v_mov_b32_e32 v76, v34
	v_mov_b32_e32 v77, v34
	v_mov_b32_e32 v78, v34
	v_mov_b32_e32 v79, v34
	v_mov_b32_e32 v80, v34
	v_mov_b32_e32 v81, v34
	v_mov_b32_e32 v90, v34
	v_mov_b32_e32 v91, v34
	v_mov_b32_e32 v92, v34
	v_mov_b32_e32 v93, v34
	v_mov_b32_e32 v94, v34
	v_mov_b32_e32 v95, v34
	v_mov_b32_e32 v96, v34
	v_mov_b32_e32 v97, v34
	v_mov_b32_e32 v98, v34
	v_mov_b32_e32 v99, v34
	v_mov_b32_e32 v100, v34
	v_mov_b32_e32 v101, v34
	v_mov_b32_e32 v102, v34
	v_mov_b32_e32 v103, v34
	v_mov_b32_e32 v104, v34
	v_mov_b32_e32 v105, v34
	v_mov_b32_e32 v114, v34
	v_mov_b32_e32 v115, v34
	v_mov_b32_e32 v116, v34
	v_mov_b32_e32 v117, v34
	v_mov_b32_e32 v118, v34
	v_mov_b32_e32 v119, v34
	v_mov_b32_e32 v120, v34
	v_mov_b32_e32 v121, v34
	v_mov_b32_e32 v130, v34
	v_mov_b32_e32 v131, v34
	v_mov_b32_e32 v132, v34
	v_mov_b32_e32 v133, v34
	v_mov_b32_e32 v134, v34
	v_mov_b32_e32 v135, v34
	v_mov_b32_e32 v136, v34
	v_mov_b32_e32 v137, v34
	v_mov_b32_e32 v146, v34
	v_mov_b32_e32 v147, v34
	v_mov_b32_e32 v148, v34
	v_mov_b32_e32 v149, v34
	v_mov_b32_e32 v150, v34
	v_mov_b32_e32 v151, v34
	v_mov_b32_e32 v152, v34
	v_mov_b32_e32 v153, v34
	v_mov_b32_e32 v106, v34
	v_mov_b32_e32 v107, v34
	v_mov_b32_e32 v108, v34
	v_mov_b32_e32 v109, v34
	v_mov_b32_e32 v110, v34
	v_mov_b32_e32 v111, v34
	v_mov_b32_e32 v112, v34
	v_mov_b32_e32 v113, v34
	v_mov_b32_e32 v122, v34
	v_mov_b32_e32 v123, v34
	v_mov_b32_e32 v124, v34
	v_mov_b32_e32 v125, v34
	v_mov_b32_e32 v126, v34
	v_mov_b32_e32 v127, v34
	v_mov_b32_e32 v128, v34
	v_mov_b32_e32 v129, v34
	v_mov_b32_e32 v138, v34
	v_mov_b32_e32 v139, v34
	v_mov_b32_e32 v140, v34
	v_mov_b32_e32 v141, v34
	v_mov_b32_e32 v142, v34
	v_mov_b32_e32 v143, v34
	v_mov_b32_e32 v144, v34
	v_mov_b32_e32 v145, v34
	v_mov_b32_e32 v154, v34
	v_mov_b32_e32 v155, v34
	v_mov_b32_e32 v156, v34
	v_mov_b32_e32 v157, v34
	v_mov_b32_e32 v158, v34
	v_mov_b32_e32 v159, v34
	v_mov_b32_e32 v160, v34
	v_mov_b32_e32 v161, v34
	s_cmp_eq_u32 s98, 0
	s_cbranch_scc1 .LBB0_1443
	ds_read_b128 v[26:29], v191
	ds_read_b128 v[30:33], v191 offset:1024
	ds_read_b128 v[18:21], v191 offset:2048
	ds_read_b128 v[22:25], v191 offset:3072
	ds_read_b128 v[10:13], v192
	ds_read_b128 v[14:17], v192 offset:1024
	ds_read_b128 v[2:5], v192 offset:2048
	ds_read_b128 v[6:9], v192 offset:3072
	s_cmp_eq_u32 s54, s23
	s_cselect_b64 vcc, -1, 0
	s_add_i32 s23, s23, 2
	s_and_b64 s[38:39], vcc, exec
	s_cselect_b32 s38, 0, s34
	s_cselect_b32 s25, 0, s35
	s_add_u32 s38, s12, s38
	s_addc_u32 s39, s13, s25
	s_add_u32 s25, s30, s34
	s_addc_u32 s67, s31, s35
	s_and_b64 s[40:41], vcc, exec
	v_cndmask_b32_e32 v168, v197, v198, vcc
	v_cndmask_b32_e32 v202, v172, v200, vcc
	v_cndmask_b32_e32 v184, v170, v199, vcc
	s_cselect_b32 s41, s27, s67
	s_cselect_b32 s40, s26, s25
	s_mov_b32 m0, s55
	v_lshl_add_u64 v[186:187], s[36:37], 0, v[172:173]
	ds_read_b128 v[176:179], v193
	ds_read_b128 v[180:183], v193 offset:1024
	ds_read_b128 v[208:211], v193 offset:2048
	ds_read_b128 v[212:215], v193 offset:3072
	ds_read_b128 v[216:219], v193 offset:4096
	ds_read_b128 v[220:223], v193 offset:5120
	ds_read_b128 v[224:227], v193 offset:6144
	ds_read_b128 v[228:231], v193 offset:7168
	global_load_lds_dwordx4 v[186:187], off
	v_lshl_add_u64 v[186:187], s[36:37], 0, v[174:175]
	s_mov_b32 m0, s56
	s_nop 0
	global_load_lds_dwordx4 v[186:187], off
	s_waitcnt vmcnt(16)
	s_waitcnt lgkmcnt(0)
	s_barrier
	s_setprio 1
	s_waitcnt lgkmcnt(0)
	v_mfma_scale_f32_16x16x128_f8f6f4 v[158:161], v[26:33], v[176:183], v[158:161], v188, v189 op_sel_hi:[0,0,0]
	v_mfma_scale_f32_16x16x128_f8f6f4 v[154:157], v[18:25], v[176:183], v[154:157], v188, v189 op_sel_hi:[0,0,0]
	v_mfma_scale_f32_16x16x128_f8f6f4 v[142:145], v[26:33], v[208:215], v[142:145], v188, v189 op_sel_hi:[0,0,0]
	v_mfma_scale_f32_16x16x128_f8f6f4 v[138:141], v[18:25], v[208:215], v[138:141], v188, v189 op_sel_hi:[0,0,0]
	v_mfma_scale_f32_16x16x128_f8f6f4 v[126:129], v[26:33], v[216:223], v[126:129], v188, v189 op_sel_hi:[0,0,0]
	v_mfma_scale_f32_16x16x128_f8f6f4 v[122:125], v[18:25], v[216:223], v[122:125], v188, v189 op_sel_hi:[0,0,0]
	v_mfma_scale_f32_16x16x128_f8f6f4 v[110:113], v[26:33], v[224:231], v[110:113], v188, v189 op_sel_hi:[0,0,0]
	v_mfma_scale_f32_16x16x128_f8f6f4 v[106:109], v[18:25], v[224:231], v[106:109], v188, v189 op_sel_hi:[0,0,0]
	s_setprio 0
	s_setprio 1
	v_mfma_scale_f32_16x16x128_f8f6f4 v[150:153], v[10:17], v[176:183], v[150:153], v188, v189 op_sel_hi:[0,0,0]
	v_mfma_scale_f32_16x16x128_f8f6f4 v[146:149], v[2:9], v[176:183], v[146:149], v188, v189 op_sel_hi:[0,0,0]
	v_mfma_scale_f32_16x16x128_f8f6f4 v[134:137], v[10:17], v[208:215], v[134:137], v188, v189 op_sel_hi:[0,0,0]
	v_mfma_scale_f32_16x16x128_f8f6f4 v[130:133], v[2:9], v[208:215], v[130:133], v188, v189 op_sel_hi:[0,0,0]
	v_mfma_scale_f32_16x16x128_f8f6f4 v[118:121], v[10:17], v[216:223], v[118:121], v188, v189 op_sel_hi:[0,0,0]
	v_mfma_scale_f32_16x16x128_f8f6f4 v[114:117], v[2:9], v[216:223], v[114:117], v188, v189 op_sel_hi:[0,0,0]
	v_mfma_scale_f32_16x16x128_f8f6f4 v[102:105], v[10:17], v[224:231], v[102:105], v188, v189 op_sel_hi:[0,0,0]
	v_mfma_scale_f32_16x16x128_f8f6f4 v[98:101], v[2:9], v[224:231], v[98:101], v188, v189 op_sel_hi:[0,0,0]
	s_setprio 0
	s_barrier
	s_mov_b32 m0, s57
	v_lshl_add_u64 v[176:177], s[40:41], 0, v[166:167]
	v_lshl_add_u64 v[178:179], s[40:41], 0, v[164:165]
	s_add_u32 s40, s40, s10
	ds_read_b128 v[208:211], v193 offset:16384
	ds_read_b128 v[212:215], v193 offset:17408
	ds_read_b128 v[216:219], v193 offset:18432
	ds_read_b128 v[220:223], v193 offset:19456
	ds_read_b128 v[224:227], v193 offset:20480
	ds_read_b128 v[228:231], v193 offset:21504
	ds_read_b128 v[232:235], v193 offset:22528
	ds_read_b128 v[236:239], v193 offset:23552
	global_load_lds_dwordx4 v[176:177], off
	s_mov_b32 m0, s58
	s_addc_u32 s41, s41, s11
	global_load_lds_dwordx4 v[178:179], off
	v_lshl_add_u64 v[180:181], s[40:41], 0, v[166:167]
	s_mov_b32 m0, s59
	v_lshl_add_u64 v[182:183], s[40:41], 0, v[164:165]
	global_load_lds_dwordx4 v[180:181], off
	s_mov_b32 m0, s60
	v_mov_b32_e32 v185, v169
	global_load_lds_dwordx4 v[182:183], off
	s_mov_b32 m0, s29
	v_lshl_add_u64 v[186:187], s[38:39], 0, v[168:169]
	global_load_lds_dwordx4 v168, s[38:39]
	s_mov_b32 m0, s46
	s_nop 0
	global_load_lds_dwordx4 v184, s[38:39]
	s_waitcnt vmcnt(16)
	s_waitcnt lgkmcnt(0)
	v_lshl_add_u64 v[184:185], s[38:39], 0, v[184:185]
	s_barrier
	s_setprio 1
	s_waitcnt lgkmcnt(0)
	v_mfma_scale_f32_16x16x128_f8f6f4 v[94:97], v[26:33], v[208:215], v[94:97], v188, v189 op_sel_hi:[0,0,0]
	v_mfma_scale_f32_16x16x128_f8f6f4 v[90:93], v[18:25], v[208:215], v[90:93], v188, v189 op_sel_hi:[0,0,0]
	v_mfma_scale_f32_16x16x128_f8f6f4 v[78:81], v[26:33], v[216:223], v[78:81], v188, v189 op_sel_hi:[0,0,0]
	v_mfma_scale_f32_16x16x128_f8f6f4 v[74:77], v[18:25], v[216:223], v[74:77], v188, v189 op_sel_hi:[0,0,0]
	v_mfma_scale_f32_16x16x128_f8f6f4 v[62:65], v[26:33], v[224:231], v[62:65], v188, v189 op_sel_hi:[0,0,0]
	v_mfma_scale_f32_16x16x128_f8f6f4 v[58:61], v[18:25], v[224:231], v[58:61], v188, v189 op_sel_hi:[0,0,0]
	v_mfma_scale_f32_16x16x128_f8f6f4 v[46:49], v[26:33], v[232:239], v[46:49], v188, v189 op_sel_hi:[0,0,0]
	v_mfma_scale_f32_16x16x128_f8f6f4 v[42:45], v[18:25], v[232:239], v[42:45], v188, v189 op_sel_hi:[0,0,0]
	s_setprio 0
	s_setprio 1
	v_mfma_scale_f32_16x16x128_f8f6f4 v[86:89], v[10:17], v[208:215], v[86:89], v188, v189 op_sel_hi:[0,0,0]
	v_mfma_scale_f32_16x16x128_f8f6f4 v[82:85], v[2:9], v[208:215], v[82:85], v188, v189 op_sel_hi:[0,0,0]
	v_mfma_scale_f32_16x16x128_f8f6f4 v[70:73], v[10:17], v[216:223], v[70:73], v188, v189 op_sel_hi:[0,0,0]
	v_mfma_scale_f32_16x16x128_f8f6f4 v[66:69], v[2:9], v[216:223], v[66:69], v188, v189 op_sel_hi:[0,0,0]
	v_mfma_scale_f32_16x16x128_f8f6f4 v[54:57], v[10:17], v[224:231], v[54:57], v188, v189 op_sel_hi:[0,0,0]
	v_mfma_scale_f32_16x16x128_f8f6f4 v[50:53], v[2:9], v[224:231], v[50:53], v188, v189 op_sel_hi:[0,0,0]
	v_mfma_scale_f32_16x16x128_f8f6f4 v[38:41], v[10:17], v[232:239], v[38:41], v188, v189 op_sel_hi:[0,0,0]
	v_mfma_scale_f32_16x16x128_f8f6f4 v[34:37], v[2:9], v[232:239], v[34:37], v188, v189 op_sel_hi:[0,0,0]
	s_setprio 0
	s_barrier
	ds_read_b128 v[26:29], v194
	ds_read_b128 v[30:33], v194 offset:1024
	ds_read_b128 v[18:21], v194 offset:2048
	ds_read_b128 v[22:25], v194 offset:3072
	ds_read_b128 v[10:13], v195
	ds_read_b128 v[14:17], v195 offset:1024
	ds_read_b128 v[2:5], v195 offset:2048
	ds_read_b128 v[6:9], v195 offset:3072
	s_mov_b32 m0, s47
	ds_read_b128 v[208:211], v193 offset:32768
	ds_read_b128 v[212:215], v193 offset:33792
	ds_read_b128 v[216:219], v193 offset:34816
	ds_read_b128 v[220:223], v193 offset:35840
	ds_read_b128 v[224:227], v193 offset:36864
	ds_read_b128 v[228:231], v193 offset:37888
	ds_read_b128 v[232:235], v193 offset:38912
	ds_read_b128 v[236:239], v193 offset:39936
	v_cndmask_b32_e32 v168, v174, v201, vcc
	global_load_lds_dwordx4 v202, s[38:39]
	s_mov_b32 m0, s48
	s_nop 0
	global_load_lds_dwordx4 v168, s[38:39]
	s_waitcnt vmcnt(8)
	s_waitcnt lgkmcnt(0)
	s_barrier
	s_setprio 1
	s_waitcnt lgkmcnt(0)
	v_mfma_scale_f32_16x16x128_f8f6f4 v[158:161], v[26:33], v[208:215], v[158:161], v188, v189 op_sel_hi:[0,0,0]
	v_mfma_scale_f32_16x16x128_f8f6f4 v[154:157], v[18:25], v[208:215], v[154:157], v188, v189 op_sel_hi:[0,0,0]
	v_mfma_scale_f32_16x16x128_f8f6f4 v[142:145], v[26:33], v[216:223], v[142:145], v188, v189 op_sel_hi:[0,0,0]
	v_mfma_scale_f32_16x16x128_f8f6f4 v[138:141], v[18:25], v[216:223], v[138:141], v188, v189 op_sel_hi:[0,0,0]
	v_mfma_scale_f32_16x16x128_f8f6f4 v[126:129], v[26:33], v[224:231], v[126:129], v188, v189 op_sel_hi:[0,0,0]
	v_mfma_scale_f32_16x16x128_f8f6f4 v[122:125], v[18:25], v[224:231], v[122:125], v188, v189 op_sel_hi:[0,0,0]
	v_mfma_scale_f32_16x16x128_f8f6f4 v[110:113], v[26:33], v[232:239], v[110:113], v188, v189 op_sel_hi:[0,0,0]
	v_mfma_scale_f32_16x16x128_f8f6f4 v[106:109], v[18:25], v[232:239], v[106:109], v188, v189 op_sel_hi:[0,0,0]
	s_setprio 0
	s_setprio 1
	v_mfma_scale_f32_16x16x128_f8f6f4 v[150:153], v[10:17], v[208:215], v[150:153], v188, v189 op_sel_hi:[0,0,0]
	v_mfma_scale_f32_16x16x128_f8f6f4 v[146:149], v[2:9], v[208:215], v[146:149], v188, v189 op_sel_hi:[0,0,0]
	v_mfma_scale_f32_16x16x128_f8f6f4 v[134:137], v[10:17], v[216:223], v[134:137], v188, v189 op_sel_hi:[0,0,0]
	v_mfma_scale_f32_16x16x128_f8f6f4 v[130:133], v[2:9], v[216:223], v[130:133], v188, v189 op_sel_hi:[0,0,0]
	v_mfma_scale_f32_16x16x128_f8f6f4 v[118:121], v[10:17], v[224:231], v[118:121], v188, v189 op_sel_hi:[0,0,0]
	v_mfma_scale_f32_16x16x128_f8f6f4 v[114:117], v[2:9], v[224:231], v[114:117], v188, v189 op_sel_hi:[0,0,0]
	v_mfma_scale_f32_16x16x128_f8f6f4 v[102:105], v[10:17], v[232:239], v[102:105], v188, v189 op_sel_hi:[0,0,0]
	v_mfma_scale_f32_16x16x128_f8f6f4 v[98:101], v[2:9], v[232:239], v[98:101], v188, v189 op_sel_hi:[0,0,0]
	s_setprio 0
	s_barrier
	s_mov_b32 m0, s61
	v_lshl_add_u64 v[176:177], v[176:177], 0, s[18:19]
	ds_read_b128 v[208:211], v193 offset:49152
	ds_read_b128 v[212:215], v193 offset:50176
	ds_read_b128 v[216:219], v193 offset:51200
	ds_read_b128 v[220:223], v193 offset:52224
	ds_read_b128 v[224:227], v193 offset:53248
	ds_read_b128 v[228:231], v193 offset:54272
	ds_read_b128 v[232:235], v193 offset:55296
	ds_read_b128 v[236:239], v193 offset:56320
	global_load_lds_dwordx4 v[176:177], off
	v_lshl_add_u64 v[176:177], v[178:179], 0, s[18:19]
	s_mov_b32 m0, s62
	s_nop 0
	global_load_lds_dwordx4 v[176:177], off
	v_lshl_add_u64 v[176:177], v[180:181], 0, s[18:19]
	s_mov_b32 m0, s63
	s_nop 0
	global_load_lds_dwordx4 v[176:177], off
	v_lshl_add_u64 v[176:177], v[182:183], 0, s[18:19]
	s_add_i32 m0, s63, 0x2000
	s_nop 0
	global_load_lds_dwordx4 v[176:177], off
	v_lshl_add_u64 v[176:177], v[186:187], 0, s[18:19]
	s_mov_b32 m0, s50
	s_nop 0
	global_load_lds_dwordx4 v[176:177], off
	v_lshl_add_u64 v[176:177], v[184:185], 0, s[18:19]
	s_mov_b32 m0, s51
	s_nop 0
	global_load_lds_dwordx4 v[176:177], off
	s_waitcnt vmcnt(8)
	s_waitcnt lgkmcnt(0)
	s_barrier
	s_setprio 1
	s_waitcnt lgkmcnt(0)
	v_mfma_scale_f32_16x16x128_f8f6f4 v[94:97], v[26:33], v[208:215], v[94:97], v188, v189 op_sel_hi:[0,0,0]
	v_mfma_scale_f32_16x16x128_f8f6f4 v[90:93], v[18:25], v[208:215], v[90:93], v188, v189 op_sel_hi:[0,0,0]
	v_mfma_scale_f32_16x16x128_f8f6f4 v[78:81], v[26:33], v[216:223], v[78:81], v188, v189 op_sel_hi:[0,0,0]
	v_mfma_scale_f32_16x16x128_f8f6f4 v[74:77], v[18:25], v[216:223], v[74:77], v188, v189 op_sel_hi:[0,0,0]
	v_mfma_scale_f32_16x16x128_f8f6f4 v[62:65], v[26:33], v[224:231], v[62:65], v188, v189 op_sel_hi:[0,0,0]
	v_mfma_scale_f32_16x16x128_f8f6f4 v[58:61], v[18:25], v[224:231], v[58:61], v188, v189 op_sel_hi:[0,0,0]
	v_mfma_scale_f32_16x16x128_f8f6f4 v[46:49], v[26:33], v[232:239], v[46:49], v188, v189 op_sel_hi:[0,0,0]
	v_mfma_scale_f32_16x16x128_f8f6f4 v[42:45], v[18:25], v[232:239], v[42:45], v188, v189 op_sel_hi:[0,0,0]
	s_setprio 0
	s_setprio 1
	v_mfma_scale_f32_16x16x128_f8f6f4 v[86:89], v[10:17], v[208:215], v[86:89], v188, v189 op_sel_hi:[0,0,0]
	v_mfma_scale_f32_16x16x128_f8f6f4 v[82:85], v[2:9], v[208:215], v[82:85], v188, v189 op_sel_hi:[0,0,0]
	v_mfma_scale_f32_16x16x128_f8f6f4 v[70:73], v[10:17], v[216:223], v[70:73], v188, v189 op_sel_hi:[0,0,0]
	v_mfma_scale_f32_16x16x128_f8f6f4 v[66:69], v[2:9], v[216:223], v[66:69], v188, v189 op_sel_hi:[0,0,0]
	v_mfma_scale_f32_16x16x128_f8f6f4 v[54:57], v[10:17], v[224:231], v[54:57], v188, v189 op_sel_hi:[0,0,0]
	v_mfma_scale_f32_16x16x128_f8f6f4 v[50:53], v[2:9], v[224:231], v[50:53], v188, v189 op_sel_hi:[0,0,0]
	v_mfma_scale_f32_16x16x128_f8f6f4 v[38:41], v[10:17], v[232:239], v[38:41], v188, v189 op_sel_hi:[0,0,0]
	v_mfma_scale_f32_16x16x128_f8f6f4 v[34:37], v[2:9], v[232:239], v[34:37], v188, v189 op_sel_hi:[0,0,0]
	s_setprio 0
	s_barrier
	s_add_u32 s34, s34, 0x100
	s_addc_u32 s35, s35, 0
	s_add_u32 s36, s36, 0x100
	s_addc_u32 s37, s37, 0
	s_cmp_ge_i32 s23, s49
	s_cbranch_scc1 .LBB0_1444

.LBB0_1446:
	s_nop 15
	s_nop 15
	s_nop 15
	s_nop 15
	s_nop 15
	s_nop 15
	v_lshl_or_b32 v10, s28, 8, v190
	v_max_f32_e32 v2, v158, v158
	v_med3_f32 v3, v2, s64, v196
	v_max_f32_e32 v2, v159, v159
	v_med3_f32 v4, v2, s64, v196
	v_mov_b32_e32 v2, v169
	v_cvt_pk_fp8_f32 v2, v3, v4
	v_max_f32_e32 v5, v160, v160
	v_max_f32_e32 v4, v161, v161
	v_med3_f32 v3, v5, s64, v196
	v_med3_f32 v4, v4, s64, v196
	v_cvt_pk_fp8_f32 v2, v3, v4 op_sel:[0,0,1]
	v_max_f32_e32 v3, v154, v154
	v_med3_f32 v4, v3, s64, v196
	v_max_f32_e32 v3, v155, v155
	v_med3_f32 v5, v3, s64, v196
	v_mov_b32_e32 v3, v169
	v_cvt_pk_fp8_f32 v3, v4, v5
	v_max_f32_e32 v6, v156, v156
	v_max_f32_e32 v5, v157, v157
	v_med3_f32 v4, v6, s64, v196
	v_med3_f32 v5, v5, s64, v196
	v_cvt_pk_fp8_f32 v3, v4, v5 op_sel:[0,0,1]
	v_max_f32_e32 v4, v150, v150
	v_med3_f32 v5, v4, s64, v196
	v_max_f32_e32 v4, v151, v151
	v_med3_f32 v6, v4, s64, v196
	v_mov_b32_e32 v4, v169
	v_cvt_pk_fp8_f32 v4, v5, v6
	v_max_f32_e32 v7, v152, v152
	v_max_f32_e32 v6, v153, v153
	v_med3_f32 v5, v7, s64, v196
	v_med3_f32 v6, v6, s64, v196
	v_cvt_pk_fp8_f32 v4, v5, v6 op_sel:[0,0,1]
	v_max_f32_e32 v5, v146, v146
	v_med3_f32 v6, v5, s64, v196
	v_max_f32_e32 v5, v147, v147
	v_med3_f32 v7, v5, s64, v196
	v_mov_b32_e32 v5, v169
	v_cvt_pk_fp8_f32 v5, v6, v7
	v_max_f32_e32 v8, v148, v148
	v_max_f32_e32 v7, v149, v149
	v_med3_f32 v6, v8, s64, v196
	v_med3_f32 v7, v7, s64, v196
	v_cvt_pk_fp8_f32 v5, v6, v7 op_sel:[0,0,1]
	v_max_f32_e32 v6, v142, v142
	v_med3_f32 v7, v6, s64, v196
	v_max_f32_e32 v6, v143, v143
	v_med3_f32 v8, v6, s64, v196
	v_mov_b32_e32 v6, v169
	v_cvt_pk_fp8_f32 v6, v7, v8
	v_max_f32_e32 v9, v144, v144
	v_max_f32_e32 v8, v145, v145
	v_med3_f32 v7, v9, s64, v196
	v_med3_f32 v8, v8, s64, v196
	v_cvt_pk_fp8_f32 v6, v7, v8 op_sel:[0,0,1]
	v_max_f32_e32 v7, v138, v138
	v_med3_f32 v8, v7, s64, v196
	v_max_f32_e32 v7, v139, v139
	v_med3_f32 v9, v7, s64, v196
	v_mov_b32_e32 v7, v169
	v_cvt_pk_fp8_f32 v7, v8, v9
	v_max_f32_e32 v11, v140, v140
	v_max_f32_e32 v9, v141, v141
	v_med3_f32 v8, v11, s64, v196
	v_med3_f32 v9, v9, s64, v196
	v_cvt_pk_fp8_f32 v7, v8, v9 op_sel:[0,0,1]
	v_max_f32_e32 v8, v134, v134
	v_med3_f32 v9, v8, s64, v196
	v_max_f32_e32 v8, v135, v135
	v_med3_f32 v11, v8, s64, v196
	v_mov_b32_e32 v8, v169
	v_cvt_pk_fp8_f32 v8, v9, v11
	v_max_f32_e32 v12, v136, v136
	v_max_f32_e32 v11, v137, v137
	v_med3_f32 v9, v12, s64, v196
	v_med3_f32 v11, v11, s64, v196
	v_cvt_pk_fp8_f32 v8, v9, v11 op_sel:[0,0,1]
	v_max_f32_e32 v9, v130, v130
	v_med3_f32 v11, v9, s64, v196
	v_max_f32_e32 v9, v131, v131
	v_med3_f32 v12, v9, s64, v196
	v_mov_b32_e32 v9, v169
	v_cvt_pk_fp8_f32 v9, v11, v12
	v_max_f32_e32 v13, v132, v132
	v_max_f32_e32 v12, v133, v133
	v_med3_f32 v11, v13, s64, v196
	v_med3_f32 v12, v12, s64, v196
	v_cvt_pk_fp8_f32 v9, v11, v12 op_sel:[0,0,1]
	s_lshl_b32 s23, s66, 19
	v_add3_u32 v10, s23, v171, v10
	buffer_store_dwordx4 v[2:5], v10, s[4:7], 0 offen
	v_max_f32_e32 v11, v108, v108
	v_max_f32_e32 v12, v104, v104
	v_add_u32_e32 v2, 0x8000, v10
	buffer_store_dwordx4 v[6:9], v2, s[4:7], 0 offen
	v_max_f32_e32 v2, v126, v126
	v_med3_f32 v3, v2, s64, v196
	v_max_f32_e32 v2, v127, v127
	v_med3_f32 v4, v2, s64, v196
	v_mov_b32_e32 v2, v169
	v_cvt_pk_fp8_f32 v2, v3, v4
	v_max_f32_e32 v5, v128, v128
	v_max_f32_e32 v4, v129, v129
	v_med3_f32 v3, v5, s64, v196
	v_med3_f32 v4, v4, s64, v196
	v_cvt_pk_fp8_f32 v2, v3, v4 op_sel:[0,0,1]
	v_max_f32_e32 v3, v122, v122
	v_med3_f32 v4, v3, s64, v196
	v_max_f32_e32 v3, v123, v123
	v_med3_f32 v5, v3, s64, v196
	v_mov_b32_e32 v3, v169
	v_cvt_pk_fp8_f32 v3, v4, v5
	v_max_f32_e32 v6, v124, v124
	v_max_f32_e32 v5, v125, v125
	v_med3_f32 v4, v6, s64, v196
	v_med3_f32 v5, v5, s64, v196
	v_cvt_pk_fp8_f32 v3, v4, v5 op_sel:[0,0,1]
	v_max_f32_e32 v4, v118, v118
	v_med3_f32 v5, v4, s64, v196
	v_max_f32_e32 v4, v119, v119
	v_med3_f32 v6, v4, s64, v196
	v_mov_b32_e32 v4, v169
	v_cvt_pk_fp8_f32 v4, v5, v6
	v_max_f32_e32 v7, v120, v120
	v_max_f32_e32 v6, v121, v121
	v_med3_f32 v5, v7, s64, v196
	v_med3_f32 v6, v6, s64, v196
	v_cvt_pk_fp8_f32 v4, v5, v6 op_sel:[0,0,1]
	v_max_f32_e32 v5, v114, v114
	v_med3_f32 v6, v5, s64, v196
	v_max_f32_e32 v5, v115, v115
	v_med3_f32 v7, v5, s64, v196
	v_mov_b32_e32 v5, v169
	v_cvt_pk_fp8_f32 v5, v6, v7
	v_max_f32_e32 v8, v116, v116
	v_max_f32_e32 v7, v117, v117
	v_med3_f32 v6, v8, s64, v196
	v_med3_f32 v7, v7, s64, v196
	v_cvt_pk_fp8_f32 v5, v6, v7 op_sel:[0,0,1]
	v_max_f32_e32 v6, v110, v110
	v_med3_f32 v7, v6, s64, v196
	v_max_f32_e32 v6, v111, v111
	v_med3_f32 v8, v6, s64, v196
	v_mov_b32_e32 v6, v169
	v_cvt_pk_fp8_f32 v6, v7, v8
	v_max_f32_e32 v9, v112, v112
	v_max_f32_e32 v8, v113, v113
	v_med3_f32 v7, v9, s64, v196
	v_med3_f32 v8, v8, s64, v196
	v_cvt_pk_fp8_f32 v6, v7, v8 op_sel:[0,0,1]
	v_max_f32_e32 v7, v106, v106
	v_med3_f32 v8, v7, s64, v196
	v_max_f32_e32 v7, v107, v107
	v_med3_f32 v9, v7, s64, v196
	v_mov_b32_e32 v7, v169
	v_cvt_pk_fp8_f32 v7, v8, v9
	v_max_f32_e32 v9, v109, v109
	v_med3_f32 v8, v11, s64, v196
	v_med3_f32 v9, v9, s64, v196
	v_cvt_pk_fp8_f32 v7, v8, v9 op_sel:[0,0,1]
	v_max_f32_e32 v8, v102, v102
	v_med3_f32 v9, v8, s64, v196
	v_max_f32_e32 v8, v103, v103
	v_med3_f32 v11, v8, s64, v196
	v_mov_b32_e32 v8, v169
	v_cvt_pk_fp8_f32 v8, v9, v11
	v_max_f32_e32 v11, v105, v105
	v_med3_f32 v9, v12, s64, v196
	v_med3_f32 v11, v11, s64, v196
	v_cvt_pk_fp8_f32 v8, v9, v11 op_sel:[0,0,1]
	v_max_f32_e32 v9, v98, v98
	v_med3_f32 v11, v9, s64, v196
	v_max_f32_e32 v9, v99, v99
	v_med3_f32 v12, v9, s64, v196
	v_mov_b32_e32 v9, v169
	v_cvt_pk_fp8_f32 v9, v11, v12
	v_max_f32_e32 v13, v100, v100
	v_max_f32_e32 v12, v101, v101
	v_med3_f32 v11, v13, s64, v196
	v_med3_f32 v12, v12, s64, v196
	v_cvt_pk_fp8_f32 v9, v11, v12 op_sel:[0,0,1]
	v_add_u32_e32 v11, 0x10000, v10
	buffer_store_dwordx4 v[2:5], v11, s[4:7], 0 offen
	v_max_f32_e32 v11, v76, v76
	v_max_f32_e32 v12, v72, v72
	v_add_u32_e32 v2, 0x18000, v10
	buffer_store_dwordx4 v[6:9], v2, s[4:7], 0 offen
	v_max_f32_e32 v2, v94, v94
	v_med3_f32 v3, v2, s64, v196
	v_max_f32_e32 v2, v95, v95
	v_med3_f32 v4, v2, s64, v196
	v_mov_b32_e32 v2, v169
	v_cvt_pk_fp8_f32 v2, v3, v4
	v_max_f32_e32 v5, v96, v96
	v_max_f32_e32 v4, v97, v97
	v_med3_f32 v3, v5, s64, v196
	v_med3_f32 v4, v4, s64, v196
	v_cvt_pk_fp8_f32 v2, v3, v4 op_sel:[0,0,1]
	v_max_f32_e32 v3, v90, v90
	v_med3_f32 v4, v3, s64, v196
	v_max_f32_e32 v3, v91, v91
	v_med3_f32 v5, v3, s64, v196
	v_mov_b32_e32 v3, v169
	v_cvt_pk_fp8_f32 v3, v4, v5
	v_max_f32_e32 v6, v92, v92
	v_max_f32_e32 v5, v93, v93
	v_med3_f32 v4, v6, s64, v196
	v_med3_f32 v5, v5, s64, v196
	v_cvt_pk_fp8_f32 v3, v4, v5 op_sel:[0,0,1]
	v_max_f32_e32 v4, v86, v86
	v_med3_f32 v5, v4, s64, v196
	v_max_f32_e32 v4, v87, v87
	v_med3_f32 v6, v4, s64, v196
	v_mov_b32_e32 v4, v169
	v_cvt_pk_fp8_f32 v4, v5, v6
	v_max_f32_e32 v7, v88, v88
	v_max_f32_e32 v6, v89, v89
	v_med3_f32 v5, v7, s64, v196
	v_med3_f32 v6, v6, s64, v196
	v_cvt_pk_fp8_f32 v4, v5, v6 op_sel:[0,0,1]
	v_max_f32_e32 v5, v82, v82
	v_med3_f32 v6, v5, s64, v196
	v_max_f32_e32 v5, v83, v83
	v_med3_f32 v7, v5, s64, v196
	v_mov_b32_e32 v5, v169
	v_cvt_pk_fp8_f32 v5, v6, v7
	v_max_f32_e32 v8, v84, v84
	v_max_f32_e32 v7, v85, v85
	v_med3_f32 v6, v8, s64, v196
	v_med3_f32 v7, v7, s64, v196
	v_cvt_pk_fp8_f32 v5, v6, v7 op_sel:[0,0,1]
	v_max_f32_e32 v6, v78, v78
	v_med3_f32 v7, v6, s64, v196
	v_max_f32_e32 v6, v79, v79
	v_med3_f32 v8, v6, s64, v196
	v_mov_b32_e32 v6, v169
	v_cvt_pk_fp8_f32 v6, v7, v8
	v_max_f32_e32 v9, v80, v80
	v_max_f32_e32 v8, v81, v81
	v_med3_f32 v7, v9, s64, v196
	v_med3_f32 v8, v8, s64, v196
	v_cvt_pk_fp8_f32 v6, v7, v8 op_sel:[0,0,1]
	v_max_f32_e32 v7, v74, v74
	v_med3_f32 v8, v7, s64, v196
	v_max_f32_e32 v7, v75, v75
	v_med3_f32 v9, v7, s64, v196
	v_mov_b32_e32 v7, v169
	v_cvt_pk_fp8_f32 v7, v8, v9
	v_max_f32_e32 v9, v77, v77
	v_med3_f32 v8, v11, s64, v196
	v_med3_f32 v9, v9, s64, v196
	v_cvt_pk_fp8_f32 v7, v8, v9 op_sel:[0,0,1]
	v_max_f32_e32 v8, v70, v70
	v_med3_f32 v9, v8, s64, v196
	v_max_f32_e32 v8, v71, v71
	v_med3_f32 v11, v8, s64, v196
	v_mov_b32_e32 v8, v169
	v_cvt_pk_fp8_f32 v8, v9, v11
	v_max_f32_e32 v11, v73, v73
	v_med3_f32 v9, v12, s64, v196
	v_med3_f32 v11, v11, s64, v196
	v_cvt_pk_fp8_f32 v8, v9, v11 op_sel:[0,0,1]
	v_max_f32_e32 v9, v66, v66
	v_med3_f32 v11, v9, s64, v196
	v_max_f32_e32 v9, v67, v67
	v_med3_f32 v12, v9, s64, v196
	v_mov_b32_e32 v9, v169
	v_cvt_pk_fp8_f32 v9, v11, v12
	v_max_f32_e32 v13, v68, v68
	v_max_f32_e32 v12, v69, v69
	v_med3_f32 v11, v13, s64, v196
	v_med3_f32 v12, v12, s64, v196
	v_cvt_pk_fp8_f32 v9, v11, v12 op_sel:[0,0,1]
	v_add_u32_e32 v11, 0x40000, v10
	buffer_store_dwordx4 v[2:5], v11, s[4:7], 0 offen
	v_max_f32_e32 v11, v44, v44
	v_max_f32_e32 v12, v40, v40
	v_add_u32_e32 v2, 0x48000, v10
	buffer_store_dwordx4 v[6:9], v2, s[4:7], 0 offen
	v_max_f32_e32 v2, v62, v62
	v_med3_f32 v3, v2, s64, v196
	v_max_f32_e32 v2, v63, v63
	v_med3_f32 v4, v2, s64, v196
	v_mov_b32_e32 v2, v169
	v_cvt_pk_fp8_f32 v2, v3, v4
	v_max_f32_e32 v5, v64, v64
	v_max_f32_e32 v4, v65, v65
	v_med3_f32 v3, v5, s64, v196
	v_med3_f32 v4, v4, s64, v196
	v_cvt_pk_fp8_f32 v2, v3, v4 op_sel:[0,0,1]
	v_max_f32_e32 v3, v58, v58
	v_med3_f32 v4, v3, s64, v196
	v_max_f32_e32 v3, v59, v59
	v_med3_f32 v5, v3, s64, v196
	v_mov_b32_e32 v3, v169
	v_cvt_pk_fp8_f32 v3, v4, v5
	v_max_f32_e32 v6, v60, v60
	v_max_f32_e32 v5, v61, v61
	v_med3_f32 v4, v6, s64, v196
	v_med3_f32 v5, v5, s64, v196
	v_cvt_pk_fp8_f32 v3, v4, v5 op_sel:[0,0,1]
	v_max_f32_e32 v4, v54, v54
	v_med3_f32 v5, v4, s64, v196
	v_max_f32_e32 v4, v55, v55
	v_med3_f32 v6, v4, s64, v196
	v_mov_b32_e32 v4, v169
	v_cvt_pk_fp8_f32 v4, v5, v6
	v_max_f32_e32 v7, v56, v56
	v_max_f32_e32 v6, v57, v57
	v_med3_f32 v5, v7, s64, v196
	v_med3_f32 v6, v6, s64, v196
	v_cvt_pk_fp8_f32 v4, v5, v6 op_sel:[0,0,1]
	v_max_f32_e32 v5, v50, v50
	v_med3_f32 v6, v5, s64, v196
	v_max_f32_e32 v5, v51, v51
	v_med3_f32 v7, v5, s64, v196
	v_mov_b32_e32 v5, v169
	v_cvt_pk_fp8_f32 v5, v6, v7
	v_max_f32_e32 v8, v52, v52
	v_max_f32_e32 v7, v53, v53
	v_med3_f32 v6, v8, s64, v196
	v_med3_f32 v7, v7, s64, v196
	v_cvt_pk_fp8_f32 v5, v6, v7 op_sel:[0,0,1]
	v_max_f32_e32 v6, v46, v46
	v_med3_f32 v7, v6, s64, v196
	v_max_f32_e32 v6, v47, v47
	v_med3_f32 v8, v6, s64, v196
	v_mov_b32_e32 v6, v169
	v_cvt_pk_fp8_f32 v6, v7, v8
	v_max_f32_e32 v9, v48, v48
	v_max_f32_e32 v8, v49, v49
	v_med3_f32 v7, v9, s64, v196
	v_med3_f32 v8, v8, s64, v196
	v_cvt_pk_fp8_f32 v6, v7, v8 op_sel:[0,0,1]
	v_max_f32_e32 v7, v42, v42
	v_med3_f32 v8, v7, s64, v196
	v_max_f32_e32 v7, v43, v43
	v_med3_f32 v9, v7, s64, v196
	v_mov_b32_e32 v7, v169
	v_cvt_pk_fp8_f32 v7, v8, v9
	v_max_f32_e32 v9, v45, v45
	v_med3_f32 v8, v11, s64, v196
	v_med3_f32 v9, v9, s64, v196
	v_cvt_pk_fp8_f32 v7, v8, v9 op_sel:[0,0,1]
	v_max_f32_e32 v8, v38, v38
	v_med3_f32 v9, v8, s64, v196
	v_max_f32_e32 v8, v39, v39
	v_med3_f32 v11, v8, s64, v196
	v_mov_b32_e32 v8, v169
	v_cvt_pk_fp8_f32 v8, v9, v11
	v_max_f32_e32 v11, v41, v41
	v_med3_f32 v9, v12, s64, v196
	v_med3_f32 v11, v11, s64, v196
	v_cvt_pk_fp8_f32 v8, v9, v11 op_sel:[0,0,1]
	v_max_f32_e32 v9, v34, v34
	v_med3_f32 v11, v9, s64, v196
	v_max_f32_e32 v9, v35, v35
	v_med3_f32 v12, v9, s64, v196
	v_mov_b32_e32 v9, v169
	v_cvt_pk_fp8_f32 v9, v11, v12
	v_max_f32_e32 v13, v36, v36
	v_max_f32_e32 v12, v37, v37
	v_med3_f32 v11, v13, s64, v196
	v_med3_f32 v12, v12, s64, v196
	v_cvt_pk_fp8_f32 v9, v11, v12 op_sel:[0,0,1]
	v_add_u32_e32 v11, 0x50000, v10
	buffer_store_dwordx4 v[2:5], v11, s[4:7], 0 offen
	s_and_b64 vcc, exec, s[2:3]
	s_mov_b64 s[2:3], -1
	v_add_u32_e32 v2, 0x58000, v10
	buffer_store_dwordx4 v[6:9], v2, s[4:7], 0 offen
	s_mov_b32 s98, 1
	s_cbranch_vccnz .LBB0_1436
	s_andn2_b64 vcc, exec, s[14:15]
	s_cbranch_vccnz .LBB0_1435
	s_barrier
	s_branch .LBB0_1435

	.amdhsa_kernel _Z10fwd_kernel4Args
		.amdhsa_group_segment_fixed_size 0
		.amdhsa_private_segment_fixed_size 0
		.amdhsa_kernarg_size 568
		.amdhsa_user_sgpr_count 2
		.amdhsa_user_sgpr_dispatch_ptr 0
		.amdhsa_user_sgpr_queue_ptr 0
		.amdhsa_user_sgpr_kernarg_segment_ptr 1
		.amdhsa_user_sgpr_dispatch_id 0
		.amdhsa_user_sgpr_kernarg_preload_length 0
		.amdhsa_user_sgpr_kernarg_preload_offset 0
		.amdhsa_user_sgpr_private_segment_size 0
		.amdhsa_uses_dynamic_stack 0
		.amdhsa_enable_private_segment 0
		.amdhsa_system_sgpr_workgroup_id_x 1
		.amdhsa_system_sgpr_workgroup_id_y 0
		.amdhsa_system_sgpr_workgroup_id_z 0
		.amdhsa_system_sgpr_workgroup_info 0
		.amdhsa_system_vgpr_workitem_id 0
		.amdhsa_next_free_vgpr 256
		.amdhsa_next_free_sgpr 102
		.amdhsa_accum_offset 256
		.amdhsa_reserve_vcc 1
		.amdhsa_float_round_mode_32 0
		.amdhsa_float_round_mode_16_64 0
		.amdhsa_float_denorm_mode_32 3
		.amdhsa_float_denorm_mode_16_64 3
		.amdhsa_dx10_clamp 1
		.amdhsa_ieee_mode 1
		.amdhsa_fp16_overflow 0
		.amdhsa_tg_split 0
		.amdhsa_exception_fp_ieee_invalid_op 0
		.amdhsa_exception_fp_denorm_src 0
		.amdhsa_exception_fp_ieee_div_zero 0
		.amdhsa_exception_fp_ieee_overflow 0
		.amdhsa_exception_fp_ieee_underflow 0
		.amdhsa_exception_fp_ieee_inexact 0
		.amdhsa_exception_int_div_zero 0
	.end_amdhsa_kernel

amdhsa.kernels:
  - .agpr_count:     0
    .args:
      - .offset:         0
        .size:           312
        .value_kind:     by_value
      - .offset:         312
        .size:           4
        .value_kind:     hidden_block_count_x
      - .offset:         316
        .size:           4
        .value_kind:     hidden_block_count_y
      - .offset:         320
        .size:           4
        .value_kind:     hidden_block_count_z
      - .offset:         324
        .size:           2
        .value_kind:     hidden_group_size_x
      - .offset:         326
        .size:           2
        .value_kind:     hidden_group_size_y
      - .offset:         328
        .size:           2
        .value_kind:     hidden_group_size_z
      - .offset:         330
        .size:           2
        .value_kind:     hidden_remainder_x
      - .offset:         332
        .size:           2
        .value_kind:     hidden_remainder_y
      - .offset:         334
        .size:           2
        .value_kind:     hidden_remainder_z
      - .offset:         352
        .size:           8
        .value_kind:     hidden_global_offset_x
      - .offset:         360
        .size:           8
        .value_kind:     hidden_global_offset_y
      - .offset:         368
        .size:           8
        .value_kind:     hidden_global_offset_z
      - .offset:         376
        .size:           2
        .value_kind:     hidden_grid_dims
      - .offset:         432
        .size:           4
        .value_kind:     hidden_dynamic_lds_size
    .group_segment_fixed_size: 0
    .kernarg_segment_align: 8
    .kernarg_segment_size: 568
    .language:       OpenCL C
    .language_version:
      - 2
      - 0
    .max_flat_workgroup_size: 512
    .name:           _Z10fwd_kernel4Args
    .private_segment_fixed_size: 0
    .sgpr_count:     108
    .sgpr_spill_count: 213
    .symbol:         _Z10fwd_kernel4Args.kd
    .uniform_work_group_size: 1
    .uses_dynamic_stack: false
    .vgpr_count:     256
    .vgpr_spill_count: 0
    .wavefront_size: 64
